# final combine part A: touch the next token's rows (indices fetched two tokens ahead) so its row loads hit L2
# baseline (speedup 1.0000x reference)
; #define LAS __attribute__((address_space(3)))
; __device__ __forceinline__ void p_final(const Args& a, const Frame& F, int half) {
;     moe_tables_load(a, F);
;     const int rowbase = half ? ((const LAS int*)(F.misc + LM_PSTART))[32] : 0;
;     const int X = 256 * ((const LAS int*)(F.misc + LM_CX))[0], tbeg = half ? X : 0, tend = half ? T : X;
;     const float* mod = (const float*)(a.ws + WS_MOD); const bf16* OUTK = (const bf16*)(a.ws + WS_OUTK);
;     const int* tok_row = (const int*)(a.ws + WS_TOK_ROW); const float* ent_w = (const float*)(a.ws + WS_ENT_W);
;     const int gw = F.bid * 8 + F.wave, NGW = F.G * 8;
;     const f32x4* fw = (const f32x4*)a.in[IN_FNW] + F.lane;
;     int rkn[4]; float wkn[4];
;     { const int t0 = tbeg + gw; if (t0 < tend) {
; #pragma unroll
;         for (int k = 0; k < 4; ++k) { rkn[k] = tok_row[t0 * 4 + k] - rowbase; wkn[k] = ent_w[t0 * 4 + k]; } } }
;     for (int t = tbeg + gw; t < tend; t += NGW) {
;         f32x4* xr = (f32x4*)(a.out + (size_t)t * D) + F.lane;
;         const u32x2* x1p = (const u32x2*)x1_row(a.out, a.ws, t) + F.lane;
;         const f32x4* g2 = (const f32x4*)(mod + (t >> 13) * 6144 + 5120) + F.lane;
;         int rk[4]; float wk[4];
; #pragma unroll
;         for (int k = 0; k < 4; ++k) { rk[k] = rkn[k]; wk[k] = wkn[k]; }
;         u32x2 ok[4][4], xw[4];
; #pragma unroll
;         for (int j = 0; j < 4; ++j) { xw[j] = x1p[64 * j];
; #pragma unroll
;             for (int k = 0; k < 4; ++k) ok[j][k] = *((const u32x2*)(OUTK + (size_t)rk[k] * D) + F.lane + 64 * j); }
.LBB0_1237:
	s_or_b64 exec, exec, s[6:7]
	s_add_i32 s4, 0, 0x22310
	v_mov_b32_e32 v1, s4
	s_waitcnt lgkmcnt(0)
	s_barrier
	ds_read_b32 v1, v1
	s_lshl_b32 s5, s2, 3
	s_waitcnt lgkmcnt(0)
	v_readfirstlane_b32 s4, v1
	s_lshl_b32 s14, s4, 8
	s_add_i32 s4, s96, s5
	s_cmp_ge_i32 s4, s14
	s_cbranch_scc1 .LBB0_1242
	s_add_u32 s15, s72, 0x900000
	s_addc_u32 s16, s73, 0
	s_add_u32 s17, s72, 0x400000
	s_addc_u32 s18, s73, 0
	s_lshl_b32 s8, s4, 2
	s_ashr_i32 s9, s8, 31
	s_lshl_b32 s6, s3, 3
	s_lshl_b64 s[8:9], s[8:9], 2
	s_add_u32 s10, s15, s8
	s_addc_u32 s11, s16, s9
	v_mov_b32_e32 v11, 0
	s_add_u32 s8, s17, s8
	s_addc_u32 s9, s18, s9
	global_load_dwordx4 v[2:5], v11, s[10:11]
	global_load_dwordx4 v[6:9], v11, s[8:9]
	v_mbcnt_lo_u32_b32 v1, -1, 0
	v_mbcnt_hi_u32_b32 v14, -1, v1
	v_and_b32_e32 v1, 64, v14
	v_add_u32_e32 v15, 64, v1
	v_xor_b32_e32 v1, 1, v14
	v_cmp_lt_i32_e32 vcc, v1, v15
	v_xor_b32_e32 v16, 2, v14
	s_add_u32 s19, s72, 0x3b200000
	v_cndmask_b32_e32 v1, v14, v1, vcc
	v_cmp_lt_i32_e32 vcc, v16, v15
	s_addc_u32 s20, s73, 0
	s_add_u32 s21, s70, 0x8000000
	v_cndmask_b32_e32 v16, v14, v16, vcc
	v_lshlrev_b32_e32 v62, 2, v16
	v_xor_b32_e32 v16, 4, v14
	v_cmp_lt_i32_e32 vcc, v16, v15
	s_addc_u32 s22, s71, 0
	s_add_i32 s7, s96, s6
	v_cndmask_b32_e32 v16, v14, v16, vcc
	v_lshlrev_b32_e32 v63, 2, v16
	v_xor_b32_e32 v16, 8, v14
	v_cmp_lt_i32_e32 vcc, v16, v15
	s_add_i32 s7, s7, s5
	s_mov_b64 s[8:9], 0x24900000
	v_cndmask_b32_e32 v16, v14, v16, vcc
	v_lshlrev_b32_e32 v64, 2, v16
	v_xor_b32_e32 v16, 16, v14
	v_cmp_lt_i32_e32 vcc, v16, v15
	s_lshl_b32 s5, s7, 2
	s_lshl_b32 s23, s3, 5
	v_cndmask_b32_e32 v16, v14, v16, vcc
	v_lshlrev_b32_e32 v65, 2, v16
	v_xor_b32_e32 v16, 32, v14
	v_cmp_lt_i32_e32 vcc, v16, v15
	v_mov_b32_e32 v15, v11
	s_ashr_i32 s7, s6, 31
	v_cndmask_b32_e32 v14, v14, v16, vcc
	v_lshlrev_b32_e32 v66, 2, v14
	v_lshlrev_b32_e32 v14, 3, v252
	v_lshl_add_u64 v[14:15], s[72:73], 0, v[14:15]
	v_lshl_add_u64 v[14:15], v[14:15], 0, s[8:9]
	s_or_b32 s8, s5, 3
	s_ashr_i32 s5, s4, 31
	s_lshl_b64 s[10:11], s[4:5], 12
	s_add_u32 s10, s70, s10
	v_lshlrev_b32_e32 v10, 4, v252
	s_addc_u32 s11, s71, s11
	v_lshl_add_u64 v[16:17], s[10:11], 0, v[10:11]
	s_mov_b64 s[10:11], 0xc00
	v_lshl_add_u64 v[12:13], s[68:69], 0, v[10:11]
	v_lshlrev_b32_e32 v1, 2, v1
	v_lshl_add_u64 v[16:17], v[16:17], 0, s[10:11]
	s_lshl_b64 s[10:11], s[6:7], 12
	v_lshlrev_b32_e32 v67, 3, v252
	s_mov_b64 s[12:13], 0x105000
	s_mov_b32 s24, 0x105000
	v_mov_b32_e32 v68, 0x358637bd
	s_mov_b32 s25, 0x800000
	global_load_dwordx4 v[120:123], v[12:13], off
	global_load_dwordx4 v[124:127], v[12:13], off offset:1024
	global_load_dwordx4 v[128:131], v[12:13], off offset:2048
	global_load_dwordx4 v[132:135], v[12:13], off offset:3072
	v_and_b32_e32 v144, 15, v252
	v_lshlrev_b32_e32 v144, 7, v144
	v_mov_b32_e32 v153, v144
	v_lshlrev_b32_e32 v145, 3, v252
	v_sub_u32_e32 v144, v144, v145
	v_ashrrev_i32_e32 v145, 31, v144
	v_lshl_add_u64 v[142:143], v[14:15], 0, v[144:145]
	v_lshrrev_b32_e32 v146, 4, v252
	v_mov_b32_e32 v140, s23
	v_lshlrev_b32_e32 v140, 2, v140
	s_mov_b32 s99, 0
	s_branch .LBB0_1240

; __device__ __forceinline__ void p_final(const Args& a, const Frame& F, int half) {
;     ...
;     for (int t = tbeg + gw; t < tend; t += NGW) {
;         f32x4* xr = (f32x4*)(a.out + (size_t)t * D) + F.lane;
;         const u32x2* x1p = (const u32x2*)x1_row(a.out, a.ws, t) + F.lane;
;         const f32x4* g2 = (const f32x4*)(mod + (t >> 13) * 6144 + 5120) + F.lane;
;         int rk[4]; float wk[4];
; #pragma unroll
;         for (int k = 0; k < 4; ++k) { rk[k] = rkn[k]; wk[k] = wkn[k]; }
;         u32x2 ok[4][4], xw[4];
; #pragma unroll
;         for (int j = 0; j < 4; ++j) { xw[j] = x1p[64 * j];
; #pragma unroll
;             for (int k = 0; k < 4; ++k) ok[j][k] = *((const u32x2*)(OUTK + (size_t)rk[k] * D) + F.lane + 64 * j); }
;         { const int tn = t + NGW; if (tn < tend) {
; #pragma unroll
;             for (int k = 0; k < 4; ++k) { rkn[k] = tok_row[tn * 4 + k] - rowbase; wkn[k] = ent_w[tn * 4 + k]; } } }
.LBB0_1240:
	s_add_i32 s9, s4, 0xffff8800
	s_cmpk_lt_i32 s4, 0x7800
	s_cselect_b32 s27, s5, 0
	s_cselect_b32 s26, s4, s9
	s_waitcnt vmcnt(4)
	v_ashrrev_i32_e32 v23, 31, v4
	v_mov_b32_e32 v22, v4
	s_cselect_b32 s9, s22, s20
	s_cselect_b32 s28, s21, s19
	s_lshl_b64 s[26:27], s[26:27], 11
	v_lshlrev_b64 v[22:23], 11, v[22:23]
	s_add_u32 s26, s28, s26
	v_ashrrev_i32_e32 v19, 31, v2
	v_mov_b32_e32 v18, v2
	v_ashrrev_i32_e32 v21, 31, v3
	v_mov_b32_e32 v20, v3
	v_lshl_add_u64 v[70:71], v[14:15], 0, v[22:23]
	v_ashrrev_i32_e32 v23, 31, v5
	v_mov_b32_e32 v22, v5
	s_addc_u32 s27, s9, s27
	v_lshlrev_b64 v[18:19], 11, v[18:19]
	v_lshlrev_b64 v[20:21], 11, v[20:21]
	v_lshlrev_b64 v[22:23], 11, v[22:23]
	v_lshl_add_u64 v[18:19], v[14:15], 0, v[18:19]
	v_lshl_add_u64 v[20:21], v[14:15], 0, v[20:21]
	v_lshl_add_u64 v[72:73], v[14:15], 0, v[22:23]
	s_add_i32 s46, s4, s6
	s_cmp_ge_i32 s46, s14
	s_cbranch_scc1 .Lp13_nt
	s_add_i32 s47, s46, 0xffff8800
	s_cmpk_lt_i32 s46, 0x7800
	s_cselect_b32 s50, s46, s47
	s_cselect_b32 s100, s21, s19
	s_cselect_b32 s101, s22, s20
	s_mov_b32 s51, 0
	s_lshl_b64 s[50:51], s[50:51], 11
	s_add_u32 s50, s100, s50
	s_addc_u32 s51, s101, s51
	global_load_dword v151, v153, s[50:51]
	s_cmp_eq_u32 s99, 0
	s_cbranch_scc1 .Lp13_nt
	v_cmp_eq_u32_e32 vcc, 1, v146
	s_nop 1
	v_cndmask_b32_e32 v148, v136, v137, vcc
	v_cmp_eq_u32_e32 vcc, 2, v146
	s_nop 1
	v_cndmask_b32_e32 v148, v148, v138, vcc
	v_cmp_eq_u32_e32 vcc, 3, v146
	s_nop 1
	v_cndmask_b32_e32 v148, v148, v139, vcc
	v_ashrrev_i32_e32 v149, 31, v148
	v_lshlrev_b64 v[148:149], 11, v[148:149]
	v_lshl_add_u64 v[148:149], v[142:143], 0, v[148:149]
	global_load_dword v150, v[148:149], off
.Lp13_nt:
	global_load_dwordx2 v[52:53], v67, s[26:27] nt
	global_load_dwordx2 v[42:43], v67, s[26:27] offset:512 nt
	global_load_dwordx2 v[32:33], v67, s[26:27] offset:1024 nt
	global_load_dwordx2 v[22:23], v67, s[26:27] offset:1536 nt
	global_load_dwordx2 v[54:55], v[18:19], off nt
	global_load_dwordx2 v[44:45], v[18:19], off offset:512 nt
	global_load_dwordx2 v[34:35], v[18:19], off offset:1024 nt
	global_load_dwordx2 v[28:29], v[18:19], off offset:1536 nt
	global_load_dwordx2 v[56:57], v[20:21], off nt
	global_load_dwordx2 v[46:47], v[20:21], off offset:512 nt
	global_load_dwordx2 v[36:37], v[20:21], off offset:1024 nt
	global_load_dwordx2 v[30:31], v[20:21], off offset:1536 nt
	global_load_dwordx2 v[58:59], v[70:71], off nt
	global_load_dwordx2 v[48:49], v[70:71], off offset:512 nt
	global_load_dwordx2 v[38:39], v[70:71], off offset:1024 nt
	global_load_dwordx2 v[24:25], v[70:71], off offset:1536 nt
	global_load_dwordx2 v[60:61], v[72:73], off nt
	global_load_dwordx2 v[50:51], v[72:73], off offset:512 nt
	global_load_dwordx2 v[40:41], v[72:73], off offset:1024 nt
	global_load_dwordx2 v[26:27], v[72:73], off offset:1536 nt
	s_add_i32 s9, s6, s4
	s_cmp_ge_i32 s9, s14
	s_waitcnt vmcnt(24)
	v_mov_b64_e32 v[20:21], v[6:7]
	v_mov_b64_e32 v[18:19], v[8:9]
	s_cbranch_scc1 .LBB0_1239
	s_add_i32 s100, s9, s6
	s_cmp_ge_i32 s100, s14
	s_cselect_b32 s101, 0, 1
	s_add_i32 s26, s8, -3
	s_ashr_i32 s27, s26, 31
	s_lshl_b64 s[26:27], s[26:27], 2
	s_add_u32 s28, s15, s26
	s_addc_u32 s29, s16, s27
	s_add_u32 s26, s17, s26
	s_addc_u32 s27, s18, s27
	s_add_i32 s34, s8, -2
	s_ashr_i32 s35, s34, 31
	s_lshl_b64 s[34:35], s[34:35], 2
	s_add_u32 s36, s15, s34
	s_addc_u32 s37, s16, s35
	s_add_u32 s34, s17, s34
	s_addc_u32 s35, s18, s35
	s_add_i32 s38, s8, -1
	s_ashr_i32 s39, s38, 31
	s_lshl_b64 s[38:39], s[38:39], 2
	s_add_u32 s40, s15, s38
	s_addc_u32 s41, s16, s39
	s_add_u32 s38, s17, s38
	s_addc_u32 s39, s18, s39
	s_ashr_i32 s9, s8, 31
	s_lshl_b64 s[42:43], s[8:9], 2
	s_add_u32 s44, s15, s42
	s_addc_u32 s45, s16, s43
	s_add_u32 s42, s17, s42
	s_addc_u32 s43, s18, s43
	global_load_dword v2, v11, s[28:29]
	global_load_dword v20, v11, s[26:27]
	global_load_dword v3, v11, s[36:37]
	global_load_dword v21, v11, s[34:35]
	global_load_dword v4, v11, s[40:41]
	global_load_dword v18, v11, s[38:39]
	global_load_dword v5, v11, s[44:45]
	global_load_dword v19, v11, s[42:43]
	s_cmp_eq_u32 s101, 0
	s_cbranch_scc1 .Lp13_nr
	global_load_dword v136, v140, s[28:29]
	global_load_dword v137, v140, s[36:37]
	global_load_dword v138, v140, s[40:41]
	global_load_dword v139, v140, s[44:45]
	s_mov_b32 s99, 1
.Lp13_nr:
	s_branch .LBB0_1239
